# speedup vs baseline: 1.0174x; 1.0174x over previous
.LBB2_54:
	v_lshlrev_b32_e32 v3, 2, v0
	v_and_b32_e32 v10, 31, v0
	v_lshrrev_b32_e32 v0, 8, v0
	v_or_b32_e32 v0, s33, v0
	s_movk_i32 s4, 0x880
	s_waitcnt lgkmcnt(0)
	v_mov_b64_e32 v[4:5], s[72:73]
	v_mad_u64_u32 v[4:5], s[0:1], v0, s4, v[4:5]
	v_and_b32_e32 v0, 0x3fc, v3
	v_cmp_lt_i32_e32 vcc, v180, v181
	v_lshlrev_b32_e32 v6, 1, v0
	v_mov_b32_e32 v7, 0
	v_cndmask_b32_e32 v0, v179, v180, vcc
	v_lshlrev_b32_e32 v0, 2, v0
	ds_bpermute_b32 v0, v0, v2
	v_lshl_add_u64 v[4:5], v[4:5], 0, v[6:7]
	s_movk_i32 s0, 0x1000
	s_waitcnt vmcnt(1)
	v_cvt_pk_f16_f32 v8, v134, v135
	v_cvt_pk_f16_f32 v9, v136, v137
	s_waitcnt lgkmcnt(0)
	v_add_f32_e32 v0, v2, v0
	v_div_scale_f32 v6, s[2:3], v0, v0, 1.0
	v_rcp_f32_e32 v11, v6
	v_add_co_u32_e32 v2, vcc, s0, v4
	global_store_dwordx2 v[4:5], v[8:9], off sc0 sc1
	s_waitcnt vmcnt(1)
	v_cvt_pk_f16_f32 v8, v130, v131
	v_cvt_pk_f16_f32 v9, v132, v133
	v_addc_co_u32_e32 v3, vcc, 0, v5, vcc
	global_store_dwordx2 v[2:3], v[8:9], off offset:256 sc0 sc1
	v_fma_f32 v2, -v6, v11, 1.0
	v_fmac_f32_e32 v11, v2, v11
	v_div_scale_f32 v2, vcc, 1.0, v0, 1.0
	v_mul_f32_e32 v3, v2, v11
	v_fma_f32 v4, -v6, v3, v2
	v_fmac_f32_e32 v3, v4, v11
	v_fma_f32 v2, -v6, v3, v2
	v_div_fmas_f32 v2, v2, v11, v3
	s_movk_i32 s0, 0x1200
	v_div_fixup_f32 v0, v2, v0, 1.0
	v_mad_u32_u24 v14, v177, s0, 0
	v_mul_u32_u24_e32 v2, 0x90, v10
	v_lshlrev_b32_e32 v3, 3, v171
	v_add3_u32 v6, v14, v2, v3
	v_pk_mul_f32 v[2:3], v[0:1], v[98:99] op_sel_hi:[0,1]
	v_pk_mul_f32 v[4:5], v[0:1], v[100:101] op_sel_hi:[0,1]
	v_cvt_pk_f16_f32 v2, v2, v3
	v_cvt_pk_f16_f32 v3, v4, v5
	v_pk_mul_f32 v[4:5], v[0:1], v[66:67] op_sel_hi:[0,1]
	v_pk_mul_f32 v[8:9], v[0:1], v[68:69] op_sel_hi:[0,1]
	v_cvt_pk_f16_f32 v4, v4, v5
	v_cvt_pk_f16_f32 v5, v8, v9
	v_pk_mul_f32 v[8:9], v[0:1], v[102:103] op_sel_hi:[0,1]
	v_pk_mul_f32 v[10:11], v[0:1], v[104:105] op_sel_hi:[0,1]
	v_cvt_pk_f16_f32 v8, v8, v9
	v_cvt_pk_f16_f32 v9, v10, v11
	v_pk_mul_f32 v[10:11], v[0:1], v[70:71] op_sel_hi:[0,1]
	v_pk_mul_f32 v[12:13], v[0:1], v[72:73] op_sel_hi:[0,1]
	s_waitcnt vmcnt(0)
	s_barrier
	v_cvt_pk_f16_f32 v10, v10, v11
	v_cvt_pk_f16_f32 v11, v12, v13
	ds_write2_b64 v6, v[2:3], v[8:9] offset1:2
	ds_write2_b64 v6, v[4:5], v[10:11] offset0:8 offset1:10
	v_pk_mul_f32 v[2:3], v[0:1], v[106:107] op_sel_hi:[0,1]
	v_pk_mul_f32 v[4:5], v[0:1], v[108:109] op_sel_hi:[0,1]
	v_cvt_pk_f16_f32 v2, v2, v3
	v_cvt_pk_f16_f32 v3, v4, v5
	v_pk_mul_f32 v[4:5], v[0:1], v[74:75] op_sel_hi:[0,1]
	v_pk_mul_f32 v[8:9], v[0:1], v[76:77] op_sel_hi:[0,1]
	v_cvt_pk_f16_f32 v4, v4, v5
	v_cvt_pk_f16_f32 v5, v8, v9
	v_pk_mul_f32 v[8:9], v[0:1], v[110:111] op_sel_hi:[0,1]
	v_pk_mul_f32 v[10:11], v[0:1], v[112:113] op_sel_hi:[0,1]
	v_cvt_pk_f16_f32 v8, v8, v9
	v_cvt_pk_f16_f32 v9, v10, v11
	v_pk_mul_f32 v[10:11], v[0:1], v[78:79] op_sel_hi:[0,1]
	v_pk_mul_f32 v[12:13], v[0:1], v[80:81] op_sel_hi:[0,1]
	v_lshlrev_b32_e32 v0, 5, v176
	v_cvt_pk_f16_f32 v10, v10, v11
	v_cvt_pk_f16_f32 v11, v12, v13
	ds_write2_b64 v6, v[2:3], v[8:9] offset0:4 offset1:6
	ds_write2_b64 v6, v[4:5], v[10:11] offset0:12 offset1:14
	v_lshl_or_b32 v0, s68, 11, v0
	v_mov_b64_e32 v[2:3], s[70:71]
	s_lshl_b32 s0, s66, 7
	v_lshrrev_b32_e32 v8, 3, v1
	s_mov_b32 s1, 0
	v_mad_i64_i32 v[2:3], s[2:3], v0, s4, v[2:3]
	s_and_b32 s0, s0, 0x780
	v_and_b32_e32 v6, 0x70, v170
	v_mul_u32_u24_e32 v0, 0x90, v8
	s_waitcnt lgkmcnt(0)
	v_lshl_add_u64 v[2:3], v[2:3], 0, s[0:1]
	v_add3_u32 v12, v14, v6, v0
	v_lshl_add_u64 v[4:5], v[2:3], 0, v[6:7]
	ds_read_b128 v[0:3], v12
	v_mul_u32_u24_e32 v6, 0x440, v8
	v_lshlrev_b32_e32 v6, 1, v6
	v_lshl_add_u64 v[8:9], v[4:5], 0, v[6:7]
	ds_read_b128 v[4:7], v12 offset:1152
	s_movk_i32 s0, 0x4000
	s_waitcnt lgkmcnt(1)
	global_store_dwordx4 v[8:9], v[0:3], off sc0 sc1
	s_nop 1
	v_add_co_u32_e32 v0, vcc, s0, v8
	s_nop 1
	v_addc_co_u32_e32 v1, vcc, 0, v9, vcc
	s_waitcnt lgkmcnt(0)
	global_store_dwordx4 v[0:1], v[4:7], off offset:1024 sc0 sc1
	ds_read_b128 v[0:3], v12 offset:2304
	ds_read_b128 v[4:7], v12 offset:3456
	v_add_co_u32_e32 v10, vcc, 0x8000, v8
	s_nop 1
	v_addc_co_u32_e32 v11, vcc, 0, v9, vcc
	s_waitcnt lgkmcnt(1)
	global_store_dwordx4 v[10:11], v[0:3], off offset:2048 sc0 sc1
	s_nop 1
	v_add_co_u32_e32 v0, vcc, 0xc000, v8
	s_nop 1
	v_addc_co_u32_e32 v1, vcc, 0, v9, vcc
	s_waitcnt lgkmcnt(0)
	global_store_dwordx4 v[0:1], v[4:7], off offset:3072 sc0 sc1
	s_endpgm
